# P3 epilogue rewritten: residual loads of all 16 blocks software-pipelined (counted vmcnt), on top of P1 epilogue de-serialisation + sc1 proj stores
# speedup vs baseline: 1.0039x; 1.0039x over previous
; __device__ __forceinline__ unsigned cvt_pk_bf16(float lo, float hi) { unsigned r; asm volatile("v_cvt_pk_bf16_f32 %0, %1, %2" : "=v"(r) : "v"(lo), "v"(hi)); return r; }
;     __device__ __forceinline__ void operator()(const f32x4 (&acc)[2][2][4][2], const Unit& u, int wr, int wc, int fr, int fq) const {
;         const int row0 = u.pm * BM + wr * 64 + fr, col0 = u.pn * BM + wc * 32 + 8 * fq;
; #pragma unroll
;         for (int bj = 0; bj < 2; ++bj) {
;             const f32x4 s0 = sb ? *(const f32x4*)(sb + col0 + bj * HALF) : (f32x4){1.f, 1.f, 1.f, 1.f}, s1 = sb ? *(const f32x4*)(sb + col0 + bj * HALF + 4) : (f32x4){1.f, 1.f, 1.f, 1.f};
; #pragma unroll
;             for (int ai = 0; ai < 2; ++ai)
; #pragma unroll
;                 for (int m = 0; m < 4; ++m) { const size_t off = (size_t)(row0 + ai * HALF + m * 16) * ldc + col0 + bj * HALF;
;                     f32x4 b0, b1;
;                     if constexpr (BF32) { b0 = *(const f32x4*)((const float*)base + off); b1 = *(const f32x4*)((const float*)base + off + 4); }
;                     else { const u32x4 bw = *(const u32x4*)(base + off);
;                         b0 = (f32x4){__uint_as_float(bw.x << 16), __uint_as_float(bw.x & 0xffff0000u), __uint_as_float(bw.y << 16), __uint_as_float(bw.y & 0xffff0000u)};
;                         b1 = (f32x4){__uint_as_float(bw.z << 16), __uint_as_float(bw.z & 0xffff0000u), __uint_as_float(bw.w << 16), __uint_as_float(bw.w & 0xffff0000u)}; }
;                     const f32x4 v0 = b0 * alpha + acc[ai][bj][m][0] * s0, v1 = b1 * alpha + acc[ai][bj][m][1] * s1;
;                     u32x4 w; w.x = cvt_pk_bf16(v0[0], v0[1]); w.y = cvt_pk_bf16(v0[2], v0[3]); w.z = cvt_pk_bf16(v1[0], v1[1]); w.w = cvt_pk_bf16(v1[2], v1[3]);
;                     *(u32x4*)(O + off) = w;
;                     asm volatile("" ::: "memory"); }
.LBB0_483:
	v_lshl_add_u32 v28, s66, 8, v186
	v_lshl_or_b32 v10, s6, 8, v187
	v_readlane_b32 s6, v243, 6
	v_readlane_b32 s7, v243, 7
	v_lshl_add_u32 v11, v28, 11, v10
	v_lshlrev_b32_e32 v10, 2, v10
	v_lshlrev_b32_e32 v20, 2, v11
	v_add_u32_e32 v21, 0x20000, v20
	v_add_u32_e32 v22, 0x40000, v20
	v_add_u32_e32 v23, 0x60000, v20
	v_add_u32_e32 v24, 0x100000, v20
	v_add_u32_e32 v25, 0x120000, v20
	v_add_u32_e32 v26, 0x140000, v20
	v_add_u32_e32 v27, 0x160000, v20
	v_readlane_b32 s78, v243, 19
	v_readlane_b32 s82, v243, 21
	v_readlane_b32 s79, v243, 20
	v_readlane_b32 s83, v243, 22
	global_load_dwordx4 v[2:5], v10, s[6:7]
	global_load_dwordx4 v[6:9], v10, s[6:7] offset:16
	global_load_dwordx4 v[12:15], v10, s[6:7] offset:512
	global_load_dwordx4 v[16:19], v10, s[6:7] offset:528
	global_load_dwordx4 v[178:181], v20, s[68:69]
	global_load_dwordx4 v[182:185], v20, s[68:69] offset:16
	global_load_dwordx4 v[190:193], v21, s[68:69]
	global_load_dwordx4 v[194:197], v21, s[68:69] offset:16
	global_load_dwordx4 v[214:217], v22, s[68:69]
	global_load_dwordx4 v[218:221], v22, s[68:69] offset:16
	global_load_dwordx4 v[222:225], v23, s[68:69]
	global_load_dwordx4 v[226:229], v23, s[68:69] offset:16
	global_load_dwordx4 v[230:233], v24, s[68:69]
	global_load_dwordx4 v[234:237], v24, s[68:69] offset:16
	global_load_dwordx4 v[238:241], v25, s[68:69]
	global_load_dwordx4 v[198:201], v25, s[68:69] offset:16
	global_load_dwordx4 v[244:247], v26, s[68:69]
	global_load_dwordx4 v[248:251], v26, s[68:69] offset:16
	global_load_dwordx4 v[252:255], v27, s[68:69]
	global_load_dwordx4 v[28:31], v27, s[68:69] offset:16
	s_waitcnt vmcnt(14)
	v_pk_mul_f32 v[178:179], v[178:179], s[52:53] op_sel_hi:[1,0]
	v_pk_mul_f32 v[180:181], v[180:181], s[52:53] op_sel_hi:[1,0]
	v_pk_mul_f32 v[182:183], v[182:183], s[52:53] op_sel_hi:[1,0]
	v_pk_mul_f32 v[184:185], v[184:185], s[52:53] op_sel_hi:[1,0]
	v_pk_fma_f32 v[178:179], v[158:159], v[2:3], v[178:179]
	v_pk_fma_f32 v[180:181], v[160:161], v[4:5], v[180:181]
	v_pk_fma_f32 v[182:183], v[154:155], v[6:7], v[182:183]
	v_pk_fma_f32 v[184:185], v[156:157], v[8:9], v[184:185]
	v_lshrrev_b32_e32 v11, 1, v20
	v_cvt_pk_bf16_f32 v178, v178, v179
	v_cvt_pk_bf16_f32 v179, v180, v181
	v_cvt_pk_bf16_f32 v180, v182, v183
	v_cvt_pk_bf16_f32 v181, v184, v185
	global_store_dwordx4 v11, v[178:181], s[0:1]
	global_load_dwordx4 v[154:157], v20, s[68:69] offset:512
	global_load_dwordx4 v[158:161], v20, s[68:69] offset:528
	s_waitcnt vmcnt(15)
	v_pk_mul_f32 v[190:191], v[190:191], s[52:53] op_sel_hi:[1,0]
	v_pk_mul_f32 v[192:193], v[192:193], s[52:53] op_sel_hi:[1,0]
	v_pk_mul_f32 v[194:195], v[194:195], s[52:53] op_sel_hi:[1,0]
	v_pk_mul_f32 v[196:197], v[196:197], s[52:53] op_sel_hi:[1,0]
	v_pk_fma_f32 v[190:191], v[150:151], v[2:3], v[190:191]
	v_pk_fma_f32 v[192:193], v[152:153], v[4:5], v[192:193]
	v_pk_fma_f32 v[194:195], v[146:147], v[6:7], v[194:195]
	v_pk_fma_f32 v[196:197], v[148:149], v[8:9], v[196:197]
	v_lshrrev_b32_e32 v11, 1, v21
	v_cvt_pk_bf16_f32 v190, v190, v191
	v_cvt_pk_bf16_f32 v191, v192, v193
	v_cvt_pk_bf16_f32 v192, v194, v195
	v_cvt_pk_bf16_f32 v193, v196, v197
	global_store_dwordx4 v11, v[190:193], s[0:1]
	global_load_dwordx4 v[146:149], v21, s[68:69] offset:512
	global_load_dwordx4 v[150:153], v21, s[68:69] offset:528
	s_waitcnt vmcnt(16)
	v_pk_mul_f32 v[214:215], v[214:215], s[52:53] op_sel_hi:[1,0]
	v_pk_mul_f32 v[216:217], v[216:217], s[52:53] op_sel_hi:[1,0]
	v_pk_mul_f32 v[218:219], v[218:219], s[52:53] op_sel_hi:[1,0]
	v_pk_mul_f32 v[220:221], v[220:221], s[52:53] op_sel_hi:[1,0]
	v_pk_fma_f32 v[214:215], v[142:143], v[2:3], v[214:215]
	v_pk_fma_f32 v[216:217], v[144:145], v[4:5], v[216:217]
	v_pk_fma_f32 v[218:219], v[138:139], v[6:7], v[218:219]
	v_pk_fma_f32 v[220:221], v[140:141], v[8:9], v[220:221]
	v_lshrrev_b32_e32 v11, 1, v22
	v_cvt_pk_bf16_f32 v214, v214, v215
	v_cvt_pk_bf16_f32 v215, v216, v217
	v_cvt_pk_bf16_f32 v216, v218, v219
	v_cvt_pk_bf16_f32 v217, v220, v221
	global_store_dwordx4 v11, v[214:217], s[0:1]
	global_load_dwordx4 v[138:141], v22, s[68:69] offset:512
	global_load_dwordx4 v[142:145], v22, s[68:69] offset:528
	s_waitcnt vmcnt(17)
	v_pk_mul_f32 v[222:223], v[222:223], s[52:53] op_sel_hi:[1,0]
	v_pk_mul_f32 v[224:225], v[224:225], s[52:53] op_sel_hi:[1,0]
	v_pk_mul_f32 v[226:227], v[226:227], s[52:53] op_sel_hi:[1,0]
	v_pk_mul_f32 v[228:229], v[228:229], s[52:53] op_sel_hi:[1,0]
	v_pk_fma_f32 v[222:223], v[134:135], v[2:3], v[222:223]
	v_pk_fma_f32 v[224:225], v[136:137], v[4:5], v[224:225]
	v_pk_fma_f32 v[226:227], v[130:131], v[6:7], v[226:227]
	v_pk_fma_f32 v[228:229], v[132:133], v[8:9], v[228:229]
	v_lshrrev_b32_e32 v11, 1, v23
	v_cvt_pk_bf16_f32 v222, v222, v223
	v_cvt_pk_bf16_f32 v223, v224, v225
	v_cvt_pk_bf16_f32 v224, v226, v227
	v_cvt_pk_bf16_f32 v225, v228, v229
	global_store_dwordx4 v11, v[222:225], s[0:1]
	global_load_dwordx4 v[130:133], v23, s[68:69] offset:512
	global_load_dwordx4 v[134:137], v23, s[68:69] offset:528
	s_waitcnt vmcnt(18)
	v_pk_mul_f32 v[230:231], v[230:231], s[52:53] op_sel_hi:[1,0]
	v_pk_mul_f32 v[232:233], v[232:233], s[52:53] op_sel_hi:[1,0]
	v_pk_mul_f32 v[234:235], v[234:235], s[52:53] op_sel_hi:[1,0]
	v_pk_mul_f32 v[236:237], v[236:237], s[52:53] op_sel_hi:[1,0]
	v_pk_fma_f32 v[230:231], v[126:127], v[2:3], v[230:231]
	v_pk_fma_f32 v[232:233], v[128:129], v[4:5], v[232:233]
	v_pk_fma_f32 v[234:235], v[122:123], v[6:7], v[234:235]
	v_pk_fma_f32 v[236:237], v[124:125], v[8:9], v[236:237]
	v_lshrrev_b32_e32 v11, 1, v24
	v_cvt_pk_bf16_f32 v230, v230, v231
	v_cvt_pk_bf16_f32 v231, v232, v233
	v_cvt_pk_bf16_f32 v232, v234, v235
	v_cvt_pk_bf16_f32 v233, v236, v237
	global_store_dwordx4 v11, v[230:233], s[0:1]
	global_load_dwordx4 v[122:125], v24, s[68:69] offset:512
	global_load_dwordx4 v[126:129], v24, s[68:69] offset:528
	s_waitcnt vmcnt(19)
; __device__ __forceinline__ unsigned cvt_pk_bf16(float lo, float hi) { unsigned r; asm volatile("v_cvt_pk_bf16_f32 %0, %1, %2" : "=v"(r) : "v"(lo), "v"(hi)); return r; }
;     __device__ __forceinline__ void operator()(const f32x4 (&acc)[2][2][4][2], const Unit& u, int wr, int wc, int fr, int fq) const {
;     ...
;             for (int ai = 0; ai < 2; ++ai)
; #pragma unroll
;                 for (int m = 0; m < 4; ++m) { const size_t off = (size_t)(row0 + ai * HALF + m * 16) * ldc + col0 + bj * HALF;
;                     f32x4 b0, b1;
;                     if constexpr (BF32) { b0 = *(const f32x4*)((const float*)base + off); b1 = *(const f32x4*)((const float*)base + off + 4); }
;                     else { const u32x4 bw = *(const u32x4*)(base + off);
;                         b0 = (f32x4){__uint_as_float(bw.x << 16), __uint_as_float(bw.x & 0xffff0000u), __uint_as_float(bw.y << 16), __uint_as_float(bw.y & 0xffff0000u)};
;                         b1 = (f32x4){__uint_as_float(bw.z << 16), __uint_as_float(bw.z & 0xffff0000u), __uint_as_float(bw.w << 16), __uint_as_float(bw.w & 0xffff0000u)}; }
;                     const f32x4 v0 = b0 * alpha + acc[ai][bj][m][0] * s0, v1 = b1 * alpha + acc[ai][bj][m][1] * s1;
;                     u32x4 w; w.x = cvt_pk_bf16(v0[0], v0[1]); w.y = cvt_pk_bf16(v0[2], v0[3]); w.z = cvt_pk_bf16(v1[0], v1[1]); w.w = cvt_pk_bf16(v1[2], v1[3]);
;                     *(u32x4*)(O + off) = w;
;                     asm volatile("" ::: "memory"); }
	v_pk_mul_f32 v[238:239], v[238:239], s[52:53] op_sel_hi:[1,0]
	v_pk_mul_f32 v[240:241], v[240:241], s[52:53] op_sel_hi:[1,0]
	v_pk_mul_f32 v[198:199], v[198:199], s[52:53] op_sel_hi:[1,0]
	v_pk_mul_f32 v[200:201], v[200:201], s[52:53] op_sel_hi:[1,0]
	v_pk_fma_f32 v[238:239], v[118:119], v[2:3], v[238:239]
	v_pk_fma_f32 v[240:241], v[120:121], v[4:5], v[240:241]
	v_pk_fma_f32 v[198:199], v[114:115], v[6:7], v[198:199]
	v_pk_fma_f32 v[200:201], v[116:117], v[8:9], v[200:201]
	v_lshrrev_b32_e32 v11, 1, v25
	v_cvt_pk_bf16_f32 v238, v238, v239
	v_cvt_pk_bf16_f32 v239, v240, v241
	v_cvt_pk_bf16_f32 v240, v198, v199
	v_cvt_pk_bf16_f32 v241, v200, v201
	global_store_dwordx4 v11, v[238:241], s[0:1]
	global_load_dwordx4 v[114:117], v25, s[68:69] offset:512
	global_load_dwordx4 v[118:121], v25, s[68:69] offset:528
	s_waitcnt vmcnt(20)
	v_pk_mul_f32 v[244:245], v[244:245], s[52:53] op_sel_hi:[1,0]
	v_pk_mul_f32 v[246:247], v[246:247], s[52:53] op_sel_hi:[1,0]
	v_pk_mul_f32 v[248:249], v[248:249], s[52:53] op_sel_hi:[1,0]
	v_pk_mul_f32 v[250:251], v[250:251], s[52:53] op_sel_hi:[1,0]
	v_pk_fma_f32 v[244:245], v[110:111], v[2:3], v[244:245]
	v_pk_fma_f32 v[246:247], v[112:113], v[4:5], v[246:247]
	v_pk_fma_f32 v[248:249], v[106:107], v[6:7], v[248:249]
	v_pk_fma_f32 v[250:251], v[108:109], v[8:9], v[250:251]
	v_lshrrev_b32_e32 v11, 1, v26
	v_cvt_pk_bf16_f32 v244, v244, v245
	v_cvt_pk_bf16_f32 v245, v246, v247
	v_cvt_pk_bf16_f32 v246, v248, v249
	v_cvt_pk_bf16_f32 v247, v250, v251
	global_store_dwordx4 v11, v[244:247], s[0:1]
	global_load_dwordx4 v[106:109], v26, s[68:69] offset:512
	global_load_dwordx4 v[110:113], v26, s[68:69] offset:528
	s_waitcnt vmcnt(21)
	v_pk_mul_f32 v[252:253], v[252:253], s[52:53] op_sel_hi:[1,0]
	v_pk_mul_f32 v[254:255], v[254:255], s[52:53] op_sel_hi:[1,0]
	v_pk_mul_f32 v[28:29], v[28:29], s[52:53] op_sel_hi:[1,0]
	v_pk_mul_f32 v[30:31], v[30:31], s[52:53] op_sel_hi:[1,0]
	v_pk_fma_f32 v[252:253], v[102:103], v[2:3], v[252:253]
	v_pk_fma_f32 v[254:255], v[104:105], v[4:5], v[254:255]
	v_pk_fma_f32 v[28:29], v[98:99], v[6:7], v[28:29]
	v_pk_fma_f32 v[30:31], v[100:101], v[8:9], v[30:31]
	v_lshrrev_b32_e32 v11, 1, v27
	v_cvt_pk_bf16_f32 v252, v252, v253
	v_cvt_pk_bf16_f32 v253, v254, v255
	v_cvt_pk_bf16_f32 v254, v28, v29
	v_cvt_pk_bf16_f32 v255, v30, v31
	global_store_dwordx4 v11, v[252:255], s[0:1]
	global_load_dwordx4 v[98:101], v27, s[68:69] offset:512
	global_load_dwordx4 v[102:105], v27, s[68:69] offset:528
	s_waitcnt vmcnt(21)
	v_pk_mul_f32 v[154:155], v[154:155], s[52:53] op_sel_hi:[1,0]
	v_pk_mul_f32 v[156:157], v[156:157], s[52:53] op_sel_hi:[1,0]
	v_pk_mul_f32 v[158:159], v[158:159], s[52:53] op_sel_hi:[1,0]
	v_pk_mul_f32 v[160:161], v[160:161], s[52:53] op_sel_hi:[1,0]
	v_pk_fma_f32 v[154:155], v[94:95], v[12:13], v[154:155]
	v_pk_fma_f32 v[156:157], v[96:97], v[14:15], v[156:157]
	v_pk_fma_f32 v[158:159], v[90:91], v[16:17], v[158:159]
	v_pk_fma_f32 v[160:161], v[92:93], v[18:19], v[160:161]
	v_lshrrev_b32_e32 v11, 1, v20
	v_cvt_pk_bf16_f32 v154, v154, v155
	v_cvt_pk_bf16_f32 v155, v156, v157
	v_cvt_pk_bf16_f32 v156, v158, v159
	v_cvt_pk_bf16_f32 v157, v160, v161
	global_store_dwordx4 v11, v[154:157], s[0:1] offset:256
	s_waitcnt vmcnt(19)
	v_pk_mul_f32 v[146:147], v[146:147], s[52:53] op_sel_hi:[1,0]
	v_pk_mul_f32 v[148:149], v[148:149], s[52:53] op_sel_hi:[1,0]
	v_pk_mul_f32 v[150:151], v[150:151], s[52:53] op_sel_hi:[1,0]
	v_pk_mul_f32 v[152:153], v[152:153], s[52:53] op_sel_hi:[1,0]
	v_pk_fma_f32 v[146:147], v[86:87], v[12:13], v[146:147]
	v_pk_fma_f32 v[148:149], v[88:89], v[14:15], v[148:149]
	v_pk_fma_f32 v[150:151], v[82:83], v[16:17], v[150:151]
	v_pk_fma_f32 v[152:153], v[84:85], v[18:19], v[152:153]
	v_lshrrev_b32_e32 v11, 1, v21
	v_cvt_pk_bf16_f32 v146, v146, v147
	v_cvt_pk_bf16_f32 v147, v148, v149
	v_cvt_pk_bf16_f32 v148, v150, v151
	v_cvt_pk_bf16_f32 v149, v152, v153
	global_store_dwordx4 v11, v[146:149], s[0:1] offset:256
	s_waitcnt vmcnt(17)
; __device__ __forceinline__ unsigned cvt_pk_bf16(float lo, float hi) { unsigned r; asm volatile("v_cvt_pk_bf16_f32 %0, %1, %2" : "=v"(r) : "v"(lo), "v"(hi)); return r; }
; #define PG8_BAR __builtin_amdgcn_s_barrier()
;     __device__ __forceinline__ void operator()(const f32x4 (&acc)[2][2][4][2], const Unit& u, int wr, int wc, int fr, int fq) const {
;     ...
;             for (int ai = 0; ai < 2; ++ai)
; #pragma unroll
;                 for (int m = 0; m < 4; ++m) { const size_t off = (size_t)(row0 + ai * HALF + m * 16) * ldc + col0 + bj * HALF;
;                     f32x4 b0, b1;
;                     if constexpr (BF32) { b0 = *(const f32x4*)((const float*)base + off); b1 = *(const f32x4*)((const float*)base + off + 4); }
;                     else { const u32x4 bw = *(const u32x4*)(base + off);
;                         b0 = (f32x4){__uint_as_float(bw.x << 16), __uint_as_float(bw.x & 0xffff0000u), __uint_as_float(bw.y << 16), __uint_as_float(bw.y & 0xffff0000u)};
;                         b1 = (f32x4){__uint_as_float(bw.z << 16), __uint_as_float(bw.z & 0xffff0000u), __uint_as_float(bw.w << 16), __uint_as_float(bw.w & 0xffff0000u)}; }
;                     const f32x4 v0 = b0 * alpha + acc[ai][bj][m][0] * s0, v1 = b1 * alpha + acc[ai][bj][m][1] * s1;
;                     u32x4 w; w.x = cvt_pk_bf16(v0[0], v0[1]); w.y = cvt_pk_bf16(v0[2], v0[3]); w.z = cvt_pk_bf16(v1[0], v1[1]); w.w = cvt_pk_bf16(v1[2], v1[3]);
;                     *(u32x4*)(O + off) = w;
;                     asm volatile("" ::: "memory"); }
;     ...
;         if constexpr (!Epi::AFTER_DRAIN) { E(acc, cur, wr, wc, fr, fq); S.done(cur); }
;         if (!has_next) break;
; #pragma unroll
;         for (int a = 0; a < 2; ++a)
; #pragma unroll
;             for (int b = 0; b < 2; ++b)
; #pragma unroll
;                 for (int m = 0; m < 4; ++m)
; #pragma unroll
;                     for (int n = 0; n < 2; ++n) acc[a][b][m][n] = (f32x4){0.f, 0.f, 0.f, 0.f};
;         cur = nxt; cA = nA; cB = nB; ++ui;
;         if constexpr (ALIGN_EPI) { if (wr == 1) PG8_BAR; }
	v_pk_mul_f32 v[138:139], v[138:139], s[52:53] op_sel_hi:[1,0]
	v_pk_mul_f32 v[140:141], v[140:141], s[52:53] op_sel_hi:[1,0]
	v_pk_mul_f32 v[142:143], v[142:143], s[52:53] op_sel_hi:[1,0]
	v_pk_mul_f32 v[144:145], v[144:145], s[52:53] op_sel_hi:[1,0]
	v_pk_fma_f32 v[138:139], v[78:79], v[12:13], v[138:139]
	v_pk_fma_f32 v[140:141], v[80:81], v[14:15], v[140:141]
	v_pk_fma_f32 v[142:143], v[74:75], v[16:17], v[142:143]
	v_pk_fma_f32 v[144:145], v[76:77], v[18:19], v[144:145]
	v_lshrrev_b32_e32 v11, 1, v22
	v_cvt_pk_bf16_f32 v138, v138, v139
	v_cvt_pk_bf16_f32 v139, v140, v141
	v_cvt_pk_bf16_f32 v140, v142, v143
	v_cvt_pk_bf16_f32 v141, v144, v145
	global_store_dwordx4 v11, v[138:141], s[0:1] offset:256
	s_waitcnt vmcnt(15)
	v_pk_mul_f32 v[130:131], v[130:131], s[52:53] op_sel_hi:[1,0]
	v_pk_mul_f32 v[132:133], v[132:133], s[52:53] op_sel_hi:[1,0]
	v_pk_mul_f32 v[134:135], v[134:135], s[52:53] op_sel_hi:[1,0]
	v_pk_mul_f32 v[136:137], v[136:137], s[52:53] op_sel_hi:[1,0]
	v_pk_fma_f32 v[130:131], v[70:71], v[12:13], v[130:131]
	v_pk_fma_f32 v[132:133], v[72:73], v[14:15], v[132:133]
	v_pk_fma_f32 v[134:135], v[66:67], v[16:17], v[134:135]
	v_pk_fma_f32 v[136:137], v[68:69], v[18:19], v[136:137]
	v_lshrrev_b32_e32 v11, 1, v23
	v_cvt_pk_bf16_f32 v130, v130, v131
	v_cvt_pk_bf16_f32 v131, v132, v133
	v_cvt_pk_bf16_f32 v132, v134, v135
	v_cvt_pk_bf16_f32 v133, v136, v137
	global_store_dwordx4 v11, v[130:133], s[0:1] offset:256
	s_waitcnt vmcnt(13)
	v_pk_mul_f32 v[122:123], v[122:123], s[52:53] op_sel_hi:[1,0]
	v_pk_mul_f32 v[124:125], v[124:125], s[52:53] op_sel_hi:[1,0]
	v_pk_mul_f32 v[126:127], v[126:127], s[52:53] op_sel_hi:[1,0]
	v_pk_mul_f32 v[128:129], v[128:129], s[52:53] op_sel_hi:[1,0]
	v_pk_fma_f32 v[122:123], v[62:63], v[12:13], v[122:123]
	v_pk_fma_f32 v[124:125], v[64:65], v[14:15], v[124:125]
	v_pk_fma_f32 v[126:127], v[58:59], v[16:17], v[126:127]
	v_pk_fma_f32 v[128:129], v[60:61], v[18:19], v[128:129]
	v_lshrrev_b32_e32 v11, 1, v24
	v_cvt_pk_bf16_f32 v122, v122, v123
	v_cvt_pk_bf16_f32 v123, v124, v125
	v_cvt_pk_bf16_f32 v124, v126, v127
	v_cvt_pk_bf16_f32 v125, v128, v129
	global_store_dwordx4 v11, v[122:125], s[0:1] offset:256
	s_waitcnt vmcnt(11)
	v_pk_mul_f32 v[114:115], v[114:115], s[52:53] op_sel_hi:[1,0]
	v_pk_mul_f32 v[116:117], v[116:117], s[52:53] op_sel_hi:[1,0]
	v_pk_mul_f32 v[118:119], v[118:119], s[52:53] op_sel_hi:[1,0]
	v_pk_mul_f32 v[120:121], v[120:121], s[52:53] op_sel_hi:[1,0]
	v_pk_fma_f32 v[114:115], v[54:55], v[12:13], v[114:115]
	v_pk_fma_f32 v[116:117], v[56:57], v[14:15], v[116:117]
	v_pk_fma_f32 v[118:119], v[50:51], v[16:17], v[118:119]
	v_pk_fma_f32 v[120:121], v[52:53], v[18:19], v[120:121]
	v_lshrrev_b32_e32 v11, 1, v25
	v_cvt_pk_bf16_f32 v114, v114, v115
	v_cvt_pk_bf16_f32 v115, v116, v117
	v_cvt_pk_bf16_f32 v116, v118, v119
	v_cvt_pk_bf16_f32 v117, v120, v121
	global_store_dwordx4 v11, v[114:117], s[0:1] offset:256
	s_waitcnt vmcnt(9)
	v_pk_mul_f32 v[106:107], v[106:107], s[52:53] op_sel_hi:[1,0]
	v_pk_mul_f32 v[108:109], v[108:109], s[52:53] op_sel_hi:[1,0]
	v_pk_mul_f32 v[110:111], v[110:111], s[52:53] op_sel_hi:[1,0]
	v_pk_mul_f32 v[112:113], v[112:113], s[52:53] op_sel_hi:[1,0]
	v_pk_fma_f32 v[106:107], v[46:47], v[12:13], v[106:107]
	v_pk_fma_f32 v[108:109], v[48:49], v[14:15], v[108:109]
	v_pk_fma_f32 v[110:111], v[42:43], v[16:17], v[110:111]
	v_pk_fma_f32 v[112:113], v[44:45], v[18:19], v[112:113]
	v_lshrrev_b32_e32 v11, 1, v26
	v_cvt_pk_bf16_f32 v106, v106, v107
	v_cvt_pk_bf16_f32 v107, v108, v109
	v_cvt_pk_bf16_f32 v108, v110, v111
	v_cvt_pk_bf16_f32 v109, v112, v113
	global_store_dwordx4 v11, v[106:109], s[0:1] offset:256
	s_waitcnt vmcnt(7)
	v_pk_mul_f32 v[98:99], v[98:99], s[52:53] op_sel_hi:[1,0]
	v_pk_mul_f32 v[100:101], v[100:101], s[52:53] op_sel_hi:[1,0]
	v_pk_mul_f32 v[102:103], v[102:103], s[52:53] op_sel_hi:[1,0]
	v_pk_mul_f32 v[104:105], v[104:105], s[52:53] op_sel_hi:[1,0]
	v_pk_fma_f32 v[98:99], v[38:39], v[12:13], v[98:99]
	v_pk_fma_f32 v[100:101], v[40:41], v[14:15], v[100:101]
	v_pk_fma_f32 v[102:103], v[34:35], v[16:17], v[102:103]
	v_pk_fma_f32 v[104:105], v[36:37], v[18:19], v[104:105]
	v_lshrrev_b32_e32 v11, 1, v27
	v_cvt_pk_bf16_f32 v98, v98, v99
	v_cvt_pk_bf16_f32 v99, v100, v101
	v_cvt_pk_bf16_f32 v100, v102, v103
	v_cvt_pk_bf16_f32 v101, v104, v105
	global_store_dwordx4 v11, v[98:101], s[0:1] offset:256
	s_andn2_b64 vcc, exec, s[38:39]
	s_mov_b64 s[6:7], -1
	s_cbranch_vccnz .LBB0_472
	s_andn2_b64 vcc, exec, s[44:45]
	s_cbranch_vccnz .LBB0_471
	s_barrier
	s_branch .LBB0_471

; __global__ void __launch_bounds__(NTHREADS, 2) mega_fwd(Ptrs P) {
;     extern __shared__ __attribute__((aligned(16))) unsigned char lds_raw[];
	.amdhsa_kernel _Z8mega_fwd4Ptrs
		.amdhsa_group_segment_fixed_size 0
		.amdhsa_private_segment_fixed_size 0
		.amdhsa_kernarg_size 424
		.amdhsa_user_sgpr_count 2
		.amdhsa_user_sgpr_dispatch_ptr 0
		.amdhsa_user_sgpr_queue_ptr 0
		.amdhsa_user_sgpr_kernarg_segment_ptr 1
		.amdhsa_user_sgpr_dispatch_id 0
		.amdhsa_user_sgpr_kernarg_preload_length 0
		.amdhsa_user_sgpr_kernarg_preload_offset 0
		.amdhsa_user_sgpr_private_segment_size 0
		.amdhsa_uses_dynamic_stack 0
		.amdhsa_enable_private_segment 0
		.amdhsa_system_sgpr_workgroup_id_x 1
		.amdhsa_system_sgpr_workgroup_id_y 0
		.amdhsa_system_sgpr_workgroup_id_z 0
		.amdhsa_system_sgpr_workgroup_info 0
		.amdhsa_system_vgpr_workitem_id 0
		.amdhsa_next_free_vgpr 256
		.amdhsa_next_free_sgpr 98
		.amdhsa_accum_offset 256
		.amdhsa_reserve_vcc 1
		.amdhsa_float_round_mode_32 0
		.amdhsa_float_round_mode_16_64 0
		.amdhsa_float_denorm_mode_32 3
		.amdhsa_float_denorm_mode_16_64 3
		.amdhsa_dx10_clamp 1
		.amdhsa_ieee_mode 1
		.amdhsa_fp16_overflow 0
		.amdhsa_tg_split 0
		.amdhsa_exception_fp_ieee_invalid_op 0
		.amdhsa_exception_fp_denorm_src 0
		.amdhsa_exception_fp_ieee_div_zero 0
		.amdhsa_exception_fp_ieee_overflow 0
		.amdhsa_exception_fp_ieee_underflow 0
		.amdhsa_exception_fp_ieee_inexact 0
		.amdhsa_exception_int_div_zero 0
	.end_amdhsa_kernel

; __global__ void __launch_bounds__(NTHREADS, 2) mega_fwd(Ptrs P) {
;     extern __shared__ __attribute__((aligned(16))) unsigned char lds_raw[];
amdhsa.kernels:
  - .agpr_count:     0
    .args:
      - .offset:         0
        .size:           168
        .value_kind:     by_value
      - .offset:         168
        .size:           4
        .value_kind:     hidden_block_count_x
      - .offset:         172
        .size:           4
        .value_kind:     hidden_block_count_y
      - .offset:         176
        .size:           4
        .value_kind:     hidden_block_count_z
      - .offset:         180
        .size:           2
        .value_kind:     hidden_group_size_x
      - .offset:         182
        .size:           2
        .value_kind:     hidden_group_size_y
      - .offset:         184
        .size:           2
        .value_kind:     hidden_group_size_z
      - .offset:         186
        .size:           2
        .value_kind:     hidden_remainder_x
      - .offset:         188
        .size:           2
        .value_kind:     hidden_remainder_y
      - .offset:         190
        .size:           2
        .value_kind:     hidden_remainder_z
      - .offset:         208
        .size:           8
        .value_kind:     hidden_global_offset_x
      - .offset:         216
        .size:           8
        .value_kind:     hidden_global_offset_y
      - .offset:         224
        .size:           8
        .value_kind:     hidden_global_offset_z
      - .offset:         232
        .size:           2
        .value_kind:     hidden_grid_dims
      - .offset:         288
        .size:           4
        .value_kind:     hidden_dynamic_lds_size
    .group_segment_fixed_size: 0
    .kernarg_segment_align: 8
    .kernarg_segment_size: 424
    .language:       OpenCL C
    .language_version:
      - 2
      - 0
    .max_flat_workgroup_size: 512
    .name:           _Z8mega_fwd4Ptrs
    .private_segment_fixed_size: 0
    .sgpr_count:     104
    .sgpr_spill_count: 95
    .symbol:         _Z8mega_fwd4Ptrs.kd
    .uniform_work_group_size: 1
    .uses_dynamic_stack: false
    .vgpr_count:     256
    .vgpr_spill_count: 0
    .wavefront_size: 64
